# speedup vs baseline: 1.0154x; 1.0063x over previous
.Lp2_poll:
	global_atomic_add v13, v17, v19, s[8:9] sc0
	s_waitcnt vmcnt(0)
	v_readfirstlane_b32 s3, v13
	s_cmpk_ge_u32 s3, 64
	s_cbranch_scc1 .Lp2_acq
	s_sleep 6
	s_add_i32 s34, s34, 1
	s_cmp_lt_u32 s34, 0x2000
	s_cbranch_scc1 .Lp2_poll
